# speedup vs baseline: 1.0099x; 1.0037x over previous
.LBB2_1:
	s_mul_i32 s22, s21, 0xe000
	v_add_u32_e32 v196, s22, v214
	v_add_u32_e32 v197, s22, v215
	s_add_u32 s46, s22, s45
	s_add_i32 s21, s21, 1
	s_waitcnt lgkmcnt(0)
	v_mfma_f32_16x16x32_f16 v[130:133], v[22:25], v[42:45], v[130:133]
	ds_read_b128 v[154:157], v196
	ds_read_b128 v[158:161], v196 offset:2048
	v_mfma_f32_16x16x32_f16 v[98:101], v[18:21], v[42:45], v[98:101]
	ds_read_b128 v[162:165], v196 offset:4096
	ds_read_b128 v[166:169], v196 offset:6144
	v_mfma_f32_16x16x32_f16 v[86:89], v[30:33], v[42:45], v[86:89]
	ds_read_b128 v[170:173], v197 offset:32768
	ds_read_b128 v[174:177], v197 offset:34816
	v_mfma_f32_16x16x32_f16 v[74:77], v[26:29], v[42:45], v[74:77]
	ds_read_b128 v[178:181], v197 offset:36864
	ds_read_b128 v[182:185], v197 offset:38912
	v_mfma_f32_16x16x32_f16 v[70:73], v[42:45], v[34:37], v[70:73]
	ds_read_b128 v[186:189], v197 offset:40960
	ds_read_b128 v[190:193], v197 offset:43008
	v_mfma_f32_16x16x32_f16 v[66:69], v[42:45], v[14:17], v[66:69]
	v_mfma_f32_16x16x32_f16 v[62:65], v[22:25], v[38:41], v[62:65]
	v_mfma_f32_16x16x32_f16 v[58:61], v[18:21], v[38:41], v[58:61]
	v_mfma_f32_16x16x32_f16 v[54:57], v[30:33], v[38:41], v[54:57]
	v_mfma_f32_16x16x32_f16 v[50:53], v[26:29], v[38:41], v[50:53]
	v_mfma_f32_16x16x32_f16 v[46:49], v[38:41], v[34:37], v[46:49]
	v_mfma_f32_16x16x32_f16 v[2:5], v[38:41], v[14:17], v[2:5]
	v_mfma_f32_16x16x32_f16 v[78:81], v[22:25], v[10:13], v[78:81]
	v_mfma_f32_16x16x32_f16 v[82:85], v[18:21], v[10:13], v[82:85]
	v_mfma_f32_16x16x32_f16 v[90:93], v[30:33], v[10:13], v[90:93]
	v_mfma_f32_16x16x32_f16 v[94:97], v[26:29], v[10:13], v[94:97]
	v_mfma_f32_16x16x32_f16 v[102:105], v[10:13], v[34:37], v[102:105]
	v_mfma_f32_16x16x32_f16 v[106:109], v[10:13], v[14:17], v[106:109]
	v_mfma_f32_16x16x32_f16 v[110:113], v[22:25], v[6:9], v[110:113]
	v_mfma_f32_16x16x32_f16 v[114:117], v[18:21], v[6:9], v[114:117]
	v_mfma_f32_16x16x32_f16 v[118:121], v[30:33], v[6:9], v[118:121]
	v_mfma_f32_16x16x32_f16 v[122:125], v[26:29], v[6:9], v[122:125]
	v_mfma_f32_16x16x32_f16 v[134:137], v[6:9], v[34:37], v[134:137]
	v_mfma_f32_16x16x32_f16 v[126:129], v[6:9], v[14:17], v[126:129]
	s_cmp_lg_u32 s21, 2
	s_cselect_b32 s21, s21, 0
	s_mul_i32 s22, s21, 0xe000
	v_add_u32_e32 v196, s22, v146
	v_add_u32_e32 v197, s22, v153
	s_waitcnt vmcnt(0) lgkmcnt(0)
	s_barrier
	v_mfma_f32_16x16x32_f16 v[130:133], v[170:173], v[154:157], v[130:133]
	ds_read_b128 v[42:45], v196
	ds_read_b128 v[38:41], v196 offset:2048
	v_mfma_f32_16x16x32_f16 v[98:101], v[174:177], v[154:157], v[98:101]
	ds_read_b128 v[10:13], v196 offset:4096
	ds_read_b128 v[6:9], v196 offset:6144
	v_mfma_f32_16x16x32_f16 v[86:89], v[178:181], v[154:157], v[86:89]
	ds_read_b128 v[22:25], v197 offset:32768
	ds_read_b128 v[18:21], v197 offset:34816
	v_mfma_f32_16x16x32_f16 v[74:77], v[182:185], v[154:157], v[74:77]
	ds_read_b128 v[30:33], v197 offset:36864
	ds_read_b128 v[26:29], v197 offset:38912
	v_mfma_f32_16x16x32_f16 v[70:73], v[154:157], v[186:189], v[70:73]
	ds_read_b128 v[34:37], v197 offset:40960
	ds_read_b128 v[14:17], v197 offset:43008
	s_mov_b32 m0, s46
	v_mfma_f32_16x16x32_f16 v[66:69], v[154:157], v[190:193], v[66:69]
	global_load_lds_dwordx4 v194, s[24:25]
	s_add_u32 m0, s46, 0x2000
	v_mfma_f32_16x16x32_f16 v[62:65], v[170:173], v[158:161], v[62:65]
	global_load_lds_dwordx4 v194, s[26:27]
	s_add_u32 m0, s46, 0x4000
	v_mfma_f32_16x16x32_f16 v[58:61], v[174:177], v[158:161], v[58:61]
	global_load_lds_dwordx4 v194, s[28:29]
	s_add_u32 m0, s46, 0x6000
	v_mfma_f32_16x16x32_f16 v[54:57], v[178:181], v[158:161], v[54:57]
	global_load_lds_dwordx4 v194, s[30:31]
	s_add_u32 m0, s46, 0x8000
	v_mfma_f32_16x16x32_f16 v[50:53], v[182:185], v[158:161], v[50:53]
	global_load_lds_dwordx4 v194, s[32:33]
	s_add_u32 m0, s46, 0xa000
	v_mfma_f32_16x16x32_f16 v[46:49], v[158:161], v[186:189], v[46:49]
	global_load_lds_dwordx4 v194, s[34:35]
	s_add_u32 m0, s46, 0xc000
	v_mfma_f32_16x16x32_f16 v[2:5], v[158:161], v[190:193], v[2:5]
	global_load_lds_dwordx4 v194, s[36:37]
	v_add_u32_e32 v194, 0x80, v194
	v_mfma_f32_16x16x32_f16 v[78:81], v[170:173], v[162:165], v[78:81]
	v_mfma_f32_16x16x32_f16 v[82:85], v[174:177], v[162:165], v[82:85]
	v_mfma_f32_16x16x32_f16 v[90:93], v[178:181], v[162:165], v[90:93]
	v_mfma_f32_16x16x32_f16 v[94:97], v[182:185], v[162:165], v[94:97]
	v_mfma_f32_16x16x32_f16 v[102:105], v[162:165], v[186:189], v[102:105]
	v_mfma_f32_16x16x32_f16 v[106:109], v[162:165], v[190:193], v[106:109]
	v_mfma_f32_16x16x32_f16 v[110:113], v[170:173], v[166:169], v[110:113]
	v_mfma_f32_16x16x32_f16 v[114:117], v[174:177], v[166:169], v[114:117]
	v_mfma_f32_16x16x32_f16 v[118:121], v[178:181], v[166:169], v[118:121]
	v_mfma_f32_16x16x32_f16 v[122:125], v[182:185], v[166:169], v[122:125]
	v_mfma_f32_16x16x32_f16 v[134:137], v[166:169], v[186:189], v[134:137]
	v_mfma_f32_16x16x32_f16 v[126:129], v[166:169], v[190:193], v[126:129]
	s_add_u32 s0, s0, 0x80
	s_addc_u32 s1, s1, 0
	s_cmpk_eq_i32 s0, 0x700
	s_cbranch_scc0 .LBB2_1
	s_waitcnt lgkmcnt(0)
	v_mfma_f32_16x16x32_f16 v[130:133], v[22:25], v[42:45], v[130:133]
	ds_read_b128 v[140:143], v214
	ds_read_b128 v[154:157], v214 offset:2048
	v_mfma_f32_16x16x32_f16 v[98:101], v[18:21], v[42:45], v[98:101]
	ds_read_b128 v[158:161], v214 offset:4096
	ds_read_b128 v[162:165], v214 offset:6144
	v_mfma_f32_16x16x32_f16 v[86:89], v[30:33], v[42:45], v[86:89]
	ds_read_b128 v[166:169], v215 offset:32768
	ds_read_b128 v[170:173], v215 offset:34816
	v_mfma_f32_16x16x32_f16 v[74:77], v[26:29], v[42:45], v[74:77]
	ds_read_b128 v[174:177], v215 offset:36864
	ds_read_b128 v[178:181], v215 offset:38912
	v_mfma_f32_16x16x32_f16 v[70:73], v[42:45], v[34:37], v[70:73]
	ds_read_b128 v[182:185], v215 offset:40960
	ds_read_b128 v[186:189], v215 offset:43008
	v_mfma_f32_16x16x32_f16 v[42:45], v[42:45], v[14:17], v[66:69]
	v_mfma_f32_16x16x32_f16 v[62:65], v[22:25], v[38:41], v[62:65]
	v_mfma_f32_16x16x32_f16 v[58:61], v[18:21], v[38:41], v[58:61]
	v_mfma_f32_16x16x32_f16 v[54:57], v[30:33], v[38:41], v[54:57]
	v_mfma_f32_16x16x32_f16 v[50:53], v[26:29], v[38:41], v[50:53]
	v_mfma_f32_16x16x32_f16 v[46:49], v[38:41], v[34:37], v[46:49]
	v_mfma_f32_16x16x32_f16 v[2:5], v[38:41], v[14:17], v[2:5]
	v_mfma_f32_16x16x32_f16 v[38:41], v[22:25], v[10:13], v[78:81]
	v_mfma_f32_16x16x32_f16 v[66:69], v[18:21], v[10:13], v[82:85]
	v_mfma_f32_16x16x32_f16 v[78:81], v[30:33], v[10:13], v[90:93]
	v_mfma_f32_16x16x32_f16 v[82:85], v[26:29], v[10:13], v[94:97]
	v_mfma_f32_16x16x32_f16 v[90:93], v[10:13], v[34:37], v[102:105]
	v_mfma_f32_16x16x32_f16 v[94:97], v[10:13], v[14:17], v[106:109]
	v_mfma_f32_16x16x32_f16 v[22:25], v[22:25], v[6:9], v[110:113]
	v_mfma_f32_16x16x32_f16 v[102:105], v[18:21], v[6:9], v[114:117]
	v_or_b32_e32 v21, v151, v152
	v_and_b32_e32 v20, 63, v0
	v_mfma_f32_16x16x32_f16 v[30:33], v[30:33], v[6:9], v[118:121]
	v_mfma_f32_16x16x32_f16 v[26:29], v[26:29], v[6:9], v[122:125]
	v_mfma_f32_16x16x32_f16 v[34:37], v[6:9], v[34:37], v[134:137]
	v_mfma_f32_16x16x32_f16 v[6:9], v[6:9], v[14:17], v[126:129]
	v_add_u32_e32 v10, 0x16800, v21
	s_waitcnt vmcnt(0) lgkmcnt(0)
	s_waitcnt lgkmcnt(0)
	v_mfma_f32_16x16x32_f16 v[16:19], v[166:169], v[140:143], v[130:133]
	s_barrier
	ds_read_b128 v[106:109], v146 offset:57344
	ds_read_b128 v[110:113], v146 offset:59392
	v_mfma_f32_16x16x32_f16 v[98:101], v[170:173], v[140:143], v[98:101]
	ds_read_b128 v[114:117], v146 offset:61440
	ds_read_b128 v[12:15], v146 offset:63488
	v_add_u32_e32 v0, 0x16000, v21
	v_mfma_f32_16x16x32_f16 v[86:89], v[174:177], v[140:143], v[86:89]
	ds_read_b128 v[122:125], v10
	v_add_u32_e32 v10, 0x17000, v21
	ds_read_b128 v[118:121], v0
	v_mfma_f32_16x16x32_f16 v[74:77], v[178:181], v[140:143], v[74:77]
	ds_read_b128 v[126:129], v10
	v_add_u32_e32 v10, 0x17800, v21
	ds_read_b128 v[130:133], v10
	v_mfma_f32_16x16x32_f16 v[70:73], v[140:143], v[182:185], v[70:73]
	ds_read_b128 v[134:137], v0 offset:8192
	ds_read_b128 v[190:193], v0 offset:10240
	v_mfma_f32_16x16x32_f16 v[42:45], v[140:143], v[186:189], v[42:45]
	v_mfma_f32_16x16x32_f16 v[62:65], v[166:169], v[154:157], v[62:65]
	v_mfma_f32_16x16x32_f16 v[58:61], v[170:173], v[154:157], v[58:61]
	v_mfma_f32_16x16x32_f16 v[54:57], v[174:177], v[154:157], v[54:57]
	v_mfma_f32_16x16x32_f16 v[50:53], v[178:181], v[154:157], v[50:53]
	v_mfma_f32_16x16x32_f16 v[46:49], v[154:157], v[182:185], v[46:49]
	v_mfma_f32_16x16x32_f16 v[140:143], v[154:157], v[186:189], v[2:5]
	v_mfma_f32_16x16x32_f16 v[38:41], v[166:169], v[158:161], v[38:41]
	v_mfma_f32_16x16x32_f16 v[66:69], v[170:173], v[158:161], v[66:69]
	v_mfma_f32_16x16x32_f16 v[78:81], v[174:177], v[158:161], v[78:81]
	v_mfma_f32_16x16x32_f16 v[82:85], v[178:181], v[158:161], v[82:85]
	v_mfma_f32_16x16x32_f16 v[90:93], v[158:161], v[182:185], v[90:93]
	v_mfma_f32_16x16x32_f16 v[94:97], v[158:161], v[186:189], v[94:97]
	v_mfma_f32_16x16x32_f16 v[22:25], v[166:169], v[162:165], v[22:25]
	v_mfma_f32_16x16x32_f16 v[102:105], v[170:173], v[162:165], v[102:105]
	v_mfma_f32_16x16x32_f16 v[30:33], v[174:177], v[162:165], v[30:33]
	v_mfma_f32_16x16x32_f16 v[26:29], v[178:181], v[162:165], v[26:29]
	v_mfma_f32_16x16x32_f16 v[34:37], v[162:165], v[182:185], v[34:37]
	v_mfma_f32_16x16x32_f16 v[152:155], v[162:165], v[186:189], v[6:9]
	s_waitcnt lgkmcnt(0)
	v_mfma_f32_16x16x32_f16 v[156:159], v[118:121], v[106:109], v[16:19]
	s_movk_i32 s0, 0x7c0
	v_add_u32_e32 v216, 0x16000, v215
	ds_read_b128 v[202:205], v216 offset:8192
	ds_read_b128 v[206:209], v216 offset:10240
	v_lshlrev_b32_e32 v16, 6, v144
	v_mov_b32_e32 v17, 0
	v_mov_b32_e32 v139, v17
	v_lshl_add_u64 v[4:5], s[6:7], 0, v[16:17]
	v_lshl_add_u64 v[8:9], v[4:5], 0, v[138:139]
	s_waitcnt vmcnt(0)
	v_lshlrev_b32_e32 v4, 5, v150
	v_lshl_add_u64 v[2:3], s[4:5], 0, v[16:17]
	v_ashrrev_i32_e32 v5, 31, v4
	v_lshl_add_u64 v[2:3], v[2:3], 0, v[138:139]
	v_lshlrev_b64 v[4:5], 2, v[4:5]
	v_lshl_add_u64 v[6:7], v[2:3], 0, v[4:5]
	v_lshl_add_u64 v[4:5], v[8:9], 0, v[4:5]
	v_mfma_f32_16x16x32_f16 v[98:101], v[122:125], v[106:109], v[98:101]
	global_load_dwordx4 v[160:163], v[6:7], off
	v_lshlrev_b32_e32 v18, 5, v147
	v_ashrrev_i32_e32 v19, 31, v18
	v_mfma_f32_16x16x32_f16 v[86:89], v[126:129], v[106:109], v[86:89]
	v_lshlrev_b64 v[18:19], 2, v[18:19]
	ds_read_b128 v[172:175], v214 offset:61440
	ds_read_b128 v[176:179], v214 offset:63488
	v_mfma_f32_16x16x32_f16 v[74:77], v[130:133], v[106:109], v[74:77]
	v_mfma_f32_16x16x32_f16 v[70:73], v[106:109], v[134:137], v[70:73]
	v_mfma_f32_16x16x32_f16 v[42:45], v[106:109], v[190:193], v[42:45]
	global_load_dwordx4 v[106:109], v[4:5], off
	v_lshlrev_b32_e32 v4, 5, v149
	v_ashrrev_i32_e32 v5, 31, v4
	v_lshlrev_b64 v[4:5], 2, v[4:5]
	v_lshl_add_u64 v[6:7], v[2:3], 0, v[4:5]
	v_lshl_add_u64 v[4:5], v[8:9], 0, v[4:5]
	global_load_dwordx4 v[168:171], v[4:5], off
	global_load_dwordx4 v[164:167], v[6:7], off
	v_lshlrev_b32_e32 v4, 5, v148
	v_ashrrev_i32_e32 v5, 31, v4
	v_lshlrev_b64 v[10:11], 2, v[4:5]
	v_lshl_add_u64 v[4:5], v[2:3], 0, v[10:11]
	v_lshl_add_u64 v[10:11], v[8:9], 0, v[10:11]
	global_load_dwordx4 v[210:213], v[10:11], off
	v_lshl_add_u64 v[2:3], v[2:3], 0, v[18:19]
	global_load_dwordx4 v[4:7], v[4:5], off
	v_lshl_add_u64 v[8:9], v[8:9], 0, v[18:19]
	v_add_u32_e32 v18, 0x16000, v215
	v_ashrrev_i32_e32 v10, 7, v145
	ds_read_b128 v[180:183], v18
	v_add_u32_e32 v18, 0x17000, v215
	v_and_b32_e32 v10, -16, v10
	v_add_u32_e32 v19, 0x16800, v215
	ds_read_b128 v[194:197], v18
	v_add_u32_e32 v18, s20, v10
	global_load_dwordx4 v[8:11], v[8:9], off
	ds_read_b128 v[184:187], v19
	v_add_u32_e32 v19, 0x17800, v215
	v_and_or_b32 v21, v145, s0, v1
	global_load_dwordx4 v[0:3], v[2:3], off
	v_mfma_f32_16x16x32_f16 v[62:65], v[118:121], v[110:113], v[62:65]
	ds_read_b128 v[198:201], v19
	v_ashrrev_i32_e32 v19, 31, v18
	ds_read_b128 v[148:151], v214 offset:59392
	v_mfma_f32_16x16x32_f16 v[58:61], v[122:125], v[110:113], v[58:61]
	v_mfma_f32_16x16x32_f16 v[54:57], v[126:129], v[110:113], v[54:57]
	v_mfma_f32_16x16x32_f16 v[50:53], v[130:133], v[110:113], v[50:53]
	v_mfma_f32_16x16x32_f16 v[46:49], v[110:113], v[134:137], v[46:49]
	v_mfma_f32_16x16x32_f16 v[110:113], v[110:113], v[190:193], v[140:143]
	s_nop 2
	ds_read_b128 v[140:143], v214 offset:57344
	v_mfma_f32_16x16x32_f16 v[38:41], v[118:121], v[114:117], v[38:41]
	v_mfma_f32_16x16x32_f16 v[66:69], v[122:125], v[114:117], v[66:69]
	v_mfma_f32_16x16x32_f16 v[78:81], v[126:129], v[114:117], v[78:81]
	v_mfma_f32_16x16x32_f16 v[82:85], v[130:133], v[114:117], v[82:85]
	v_mfma_f32_16x16x32_f16 v[90:93], v[114:117], v[134:137], v[90:93]
	v_mfma_f32_16x16x32_f16 v[94:97], v[114:117], v[190:193], v[94:97]
	s_waitcnt lgkmcnt(0)
	v_mfma_f32_16x16x32_f16 v[114:117], v[180:183], v[140:143], v[156:159]
	v_mfma_f32_16x16x32_f16 v[98:101], v[184:187], v[140:143], v[98:101]
	v_mfma_f32_16x16x32_f16 v[22:25], v[118:121], v[12:15], v[22:25]
	s_waitcnt vmcnt(6)
	s_nop 4
	v_pk_mul_f32 v[120:121], v[114:115], v[106:107] op_sel_hi:[1,0]
	v_lshlrev_b64 v[118:119], 17, v[18:19]
	v_lshl_or_b32 v118, v21, 6, v118
	v_mfma_f32_16x16x32_f16 v[102:105], v[122:125], v[12:15], v[102:105]
	v_mul_f32_e64 v122, v116, v107
	v_mul_f32_e64 v123, v117, v107
	v_pk_fma_f32 v[124:125], v[114:115], v[160:161], v[120:121] op_sel:[0,0,1] op_sel_hi:[1,1,0] neg_lo:[0,0,1] neg_hi:[0,0,1]
	v_pk_fma_f32 v[114:115], v[114:115], v[160:161], v[120:121] op_sel:[0,0,1] op_sel_hi:[1,0,0]
	v_pk_fma_f32 v[120:121], v[116:117], v[160:161], v[122:123] op_sel:[0,1,1] op_sel_hi:[1,1,0] neg_lo:[0,0,1] neg_hi:[0,0,1]
	v_pk_fma_f32 v[116:117], v[116:117], v[160:161], v[122:123] op_sel:[0,1,1] op_sel_hi:[1,1,0]
	v_cvt_pk_f16_f32 v114, v124, v115
	v_cvt_pk_f16_f32 v115, v120, v117
	v_pk_mul_f32 v[116:117], v[98:99], v[108:109] op_sel_hi:[1,0]
	v_mov_b32_e32 v122, v163
	v_pk_fma_f32 v[120:121], v[98:99], v[162:163], v[116:117] op_sel:[0,0,1] op_sel_hi:[1,1,0] neg_lo:[0,0,1] neg_hi:[0,0,1]
	v_pk_fma_f32 v[98:99], v[98:99], v[162:163], v[116:117] op_sel:[0,0,1] op_sel_hi:[1,0,0]
	v_mfma_f32_16x16x32_f16 v[30:33], v[126:129], v[12:15], v[30:33]
	v_cvt_pk_f16_f32 v116, v120, v99
	v_mov_b32_e32 v120, v109
	v_pk_mul_f32 v[98:99], v[100:101], v[120:121] op_sel_hi:[1,0]
	v_mfma_f32_16x16x32_f16 v[26:29], v[130:133], v[12:15], v[26:29]
	v_fma_f32 v124, v100, v122, -v99
	v_fma_f32 v125, v101, v122, -v98
	v_pk_fma_f32 v[98:99], v[100:101], v[122:123], v[98:99] op_sel:[0,0,1] op_sel_hi:[1,0,0]
	s_nop 0
	v_cvt_pk_f16_f32 v117, v124, v99
	v_lshlrev_b64 v[124:125], 1, v[118:119]
	v_lshl_add_u64 v[126:127], s[10:11], 0, v[124:125]
	v_mfma_f32_16x16x32_f16 v[34:37], v[12:15], v[134:137], v[34:37]
	v_mfma_f32_16x16x32_f16 v[98:101], v[12:15], v[190:193], v[152:155]
	v_lshl_add_u64 v[12:13], v[126:127], 0, v[16:17]
	v_lshl_add_u64 v[126:127], v[12:13], 0, v[138:139]
	global_store_dwordx4 v[126:127], v[114:117], off sc1
	v_mfma_f32_16x16x32_f16 v[12:15], v[194:197], v[140:143], v[86:89]
	v_mfma_f32_16x16x32_f16 v[74:77], v[198:201], v[140:143], v[74:77]
	v_mfma_f32_16x16x32_f16 v[58:61], v[184:187], v[148:151], v[58:61]
	s_nop 5
	v_mul_f32_e64 v86, v12, v106
	v_mul_f32_e64 v87, v13, v106
	v_pk_fma_f32 v[88:89], v[12:13], v[160:161], v[86:87] op_sel:[0,0,1] op_sel_hi:[1,1,0] neg_lo:[0,0,1] neg_hi:[0,0,1]
	v_pk_fma_f32 v[12:13], v[12:13], v[160:161], v[86:87] op_sel:[0,0,1] op_sel_hi:[1,0,0]
	v_mfma_f32_16x16x32_f16 v[54:57], v[194:197], v[148:151], v[54:57]
	v_cvt_pk_f16_f32 v86, v88, v13
	v_pk_mul_f32 v[12:13], v[14:15], v[106:107] op_sel:[0,1]
	s_nop 0
	v_pk_fma_f32 v[88:89], v[14:15], v[160:161], v[12:13] op_sel:[0,1,1] op_sel_hi:[1,1,0] neg_lo:[0,0,1] neg_hi:[0,0,1]
	v_pk_fma_f32 v[12:13], v[14:15], v[160:161], v[12:13] op_sel:[0,1,1] op_sel_hi:[1,1,0]
	v_mfma_f32_16x16x32_f16 v[50:53], v[198:201], v[148:151], v[50:53]
	v_cvt_pk_f16_f32 v87, v88, v13
	v_pk_mul_f32 v[88:89], v[74:75], v[108:109] op_sel_hi:[1,0]
	v_mfma_f32_16x16x32_f16 v[12:15], v[140:143], v[206:209], v[42:45]
	s_nop 2
	v_fma_f32 v42, v74, v162, -v89
	v_fma_f32 v43, v75, v163, -v88
	v_pk_fma_f32 v[44:45], v[74:75], v[162:163], v[88:89] op_sel:[0,0,1] op_sel_hi:[1,0,0]
	v_mfma_f32_16x16x32_f16 v[38:41], v[180:183], v[172:175], v[38:41]
	v_cvt_pk_f16_f32 v88, v42, v45
	v_mfma_f32_16x16x32_f16 v[42:45], v[180:183], v[148:151], v[62:65]
	s_nop 2
	v_mul_f32_e64 v62, v76, v120
	v_mul_f32_e64 v63, v77, v120
	v_mfma_f32_16x16x32_f16 v[66:69], v[184:187], v[172:175], v[66:69]
	v_fma_f32 v64, v76, v122, -v63
	v_fma_f32 v65, v77, v122, -v62
	v_pk_fma_f32 v[62:63], v[76:77], v[122:123], v[62:63] op_sel:[0,0,1] op_sel_hi:[1,0,0]
	s_nop 0
	v_cvt_pk_f16_f32 v89, v64, v63
	v_lshl_add_u64 v[62:63], s[12:13], 0, v[124:125]
	v_lshl_add_u64 v[62:63], v[62:63], 0, v[16:17]
	v_lshl_add_u64 v[106:107], v[62:63], 0, v[138:139]
	s_waitcnt vmcnt(6)
	v_pk_mul_f32 v[62:63], v[42:43], v[168:169] op_sel_hi:[1,0]
	global_store_dwordx4 v[106:107], v[86:89], off sc1
	s_waitcnt vmcnt(6)
	v_pk_fma_f32 v[64:65], v[42:43], v[164:165], v[62:63] op_sel:[0,0,1] op_sel_hi:[1,1,0] neg_lo:[0,0,1] neg_hi:[0,0,1]
	v_pk_fma_f32 v[42:43], v[42:43], v[164:165], v[62:63] op_sel:[0,0,1] op_sel_hi:[1,0,0]
	v_pk_mul_f32 v[62:63], v[44:45], v[168:169] op_sel:[0,1]
	v_cvt_pk_f16_f32 v42, v64, v43
	v_pk_fma_f32 v[74:75], v[44:45], v[164:165], v[62:63] op_sel:[0,1,1] op_sel_hi:[1,1,0] neg_lo:[0,0,1] neg_hi:[0,0,1]
	v_pk_fma_f32 v[44:45], v[44:45], v[164:165], v[62:63] op_sel:[0,1,1] op_sel_hi:[1,1,0]
	v_mov_b32_e32 v86, v171
	v_cvt_pk_f16_f32 v43, v74, v45
	v_pk_mul_f32 v[44:45], v[58:59], v[170:171] op_sel_hi:[1,0]
	v_mov_b32_e32 v88, v167
	v_pk_fma_f32 v[74:75], v[58:59], v[166:167], v[44:45] op_sel:[0,0,1] op_sel_hi:[1,1,0] neg_lo:[0,0,1] neg_hi:[0,0,1]
	v_pk_fma_f32 v[44:45], v[58:59], v[166:167], v[44:45] op_sel:[0,0,1] op_sel_hi:[1,0,0]
	v_pk_mul_f32 v[58:59], v[60:61], v[86:87] op_sel_hi:[1,0]
	v_cvt_pk_f16_f32 v44, v74, v45
	v_pk_fma_f32 v[108:109], v[60:61], v[88:89], v[58:59] op_sel:[0,0,1] op_sel_hi:[1,0,0] neg_lo:[0,0,1] neg_hi:[0,0,1]
	v_pk_fma_f32 v[58:59], v[60:61], v[88:89], v[58:59] op_sel:[0,0,1] op_sel_hi:[1,0,0]
	v_mfma_f32_16x16x32_f16 v[74:77], v[194:197], v[172:175], v[78:81]
	v_cvt_pk_f16_f32 v45, v108, v59
	global_store_dwordx4 v[126:127], v[42:45], off offset:2048 sc1
	v_pk_mul_f32 v[58:59], v[54:55], v[168:169] op_sel_hi:[1,0]
	v_mfma_f32_16x16x32_f16 v[22:25], v[180:183], v[176:179], v[22:25]
	v_fma_f32 v78, v54, v164, -v59
	v_fma_f32 v79, v55, v165, -v58
	v_pk_fma_f32 v[54:55], v[54:55], v[164:165], v[58:59] op_sel:[0,0,1] op_sel_hi:[1,0,0]
	v_mfma_f32_16x16x32_f16 v[42:45], v[198:201], v[172:175], v[82:85]
	v_cvt_pk_f16_f32 v54, v78, v55
	s_nop 1
	v_pk_mul_f32 v[82:83], v[56:57], v[168:169] op_sel:[0,1]
	v_mfma_f32_16x16x32_f16 v[30:33], v[194:197], v[176:179], v[30:33]
	v_fma_f32 v84, v56, v165, -v83
	v_fma_f32 v85, v57, v165, -v82
	v_pk_fma_f32 v[56:57], v[56:57], v[164:165], v[82:83] op_sel:[0,1,1] op_sel_hi:[1,1,0]
	s_nop 0
	v_cvt_pk_f16_f32 v55, v84, v57
	v_pk_mul_f32 v[56:57], v[50:51], v[170:171] op_sel_hi:[1,0]
	v_mfma_f32_16x16x32_f16 v[26:29], v[198:201], v[176:179], v[26:29]
	v_fma_f32 v82, v50, v166, -v57
	v_fma_f32 v83, v51, v167, -v56
	v_pk_fma_f32 v[50:51], v[50:51], v[166:167], v[56:57] op_sel:[0,0,1] op_sel_hi:[1,0,0]
	s_nop 0
	v_cvt_pk_f16_f32 v56, v82, v51
	v_pk_mul_f32 v[50:51], v[52:53], v[86:87] op_sel_hi:[1,0]
	v_mfma_f32_16x16x32_f16 v[82:85], v[184:187], v[176:179], v[102:105]
	v_fma_f32 v86, v52, v88, -v51
	v_fma_f32 v87, v53, v88, -v50
	v_pk_fma_f32 v[50:51], v[52:53], v[88:89], v[50:51] op_sel:[0,0,1] op_sel_hi:[1,0,0]
	s_nop 0
	v_cvt_pk_f16_f32 v57, v86, v51
	global_store_dwordx4 v[106:107], v[54:57], off offset:2048 sc1
	s_waitcnt vmcnt(7)
	v_pk_mul_f32 v[50:51], v[38:39], v[210:211] op_sel_hi:[1,0]
	v_mfma_f32_16x16x32_f16 v[70:73], v[140:143], v[202:205], v[70:73]
	v_mul_f32_e64 v56, v40, v211
	v_mul_f32_e64 v57, v41, v211
	s_waitcnt vmcnt(6)
	v_pk_fma_f32 v[52:53], v[38:39], v[4:5], v[50:51] op_sel:[0,0,1] op_sel_hi:[1,1,0] neg_lo:[0,0,1] neg_hi:[0,0,1]
	v_pk_fma_f32 v[38:39], v[38:39], v[4:5], v[50:51] op_sel:[0,0,1] op_sel_hi:[1,0,0]
	v_pk_fma_f32 v[86:87], v[40:41], v[4:5], v[56:57] op_sel:[0,1,1] op_sel_hi:[1,1,0] neg_lo:[0,0,1] neg_hi:[0,0,1]
	v_pk_fma_f32 v[40:41], v[40:41], v[4:5], v[56:57] op_sel:[0,1,1] op_sel_hi:[1,1,0]
	v_cvt_pk_f16_f32 v38, v52, v39
	v_cvt_pk_f16_f32 v39, v86, v41
	v_pk_mul_f32 v[40:41], v[66:67], v[212:213] op_sel_hi:[1,0]
	v_or_b32_e32 v54, 0x800, v118
	v_pk_fma_f32 v[56:57], v[66:67], v[6:7], v[40:41] op_sel:[0,0,1] op_sel_hi:[1,1,0] neg_lo:[0,0,1] neg_hi:[0,0,1]
	v_pk_fma_f32 v[40:41], v[66:67], v[6:7], v[40:41] op_sel:[0,0,1] op_sel_hi:[1,0,0]
	v_mov_b32_e32 v55, v119
	v_cvt_pk_f16_f32 v40, v56, v41
	v_mov_b32_e32 v56, v213
	v_pk_mul_f32 v[66:67], v[68:69], v[56:57] op_sel_hi:[1,0]
	v_mov_b32_e32 v86, v7
	v_pk_fma_f32 v[88:89], v[68:69], v[86:87], v[66:67] op_sel:[0,0,1] op_sel_hi:[1,0,0] neg_lo:[0,0,1] neg_hi:[0,0,1]
	v_pk_fma_f32 v[66:67], v[68:69], v[86:87], v[66:67] op_sel:[0,0,1] op_sel_hi:[1,0,0]
	v_lshlrev_b64 v[54:55], 1, v[54:55]
	v_cvt_pk_f16_f32 v41, v88, v67
	v_lshl_add_u64 v[66:67], s[10:11], 0, v[54:55]
	v_lshl_add_u64 v[66:67], v[66:67], 0, v[16:17]
	v_lshl_add_u64 v[66:67], v[66:67], 0, v[138:139]
	global_store_dwordx4 v[66:67], v[38:41], off sc1
	v_or_b32_e32 v118, 0xc00, v118
	v_mfma_f32_16x16x32_f16 v[46:49], v[148:151], v[202:205], v[46:49]
	v_mul_f32_e64 v38, v74, v210
	v_mul_f32_e64 v39, v75, v210
	v_pk_fma_f32 v[40:41], v[74:75], v[4:5], v[38:39] op_sel:[0,0,1] op_sel_hi:[1,1,0] neg_lo:[0,0,1] neg_hi:[0,0,1]
	v_pk_fma_f32 v[38:39], v[74:75], v[4:5], v[38:39] op_sel:[0,0,1] op_sel_hi:[1,0,0]
	v_mfma_f32_16x16x32_f16 v[58:61], v[172:175], v[202:205], v[90:93]
	v_cvt_pk_f16_f32 v38, v40, v39
	v_pk_mul_f32 v[40:41], v[76:77], v[210:211] op_sel:[0,1]
	s_nop 0
	v_pk_fma_f32 v[66:67], v[76:77], v[4:5], v[40:41] op_sel:[0,1,1] op_sel_hi:[1,1,0] neg_lo:[0,0,1] neg_hi:[0,0,1]
	v_pk_fma_f32 v[4:5], v[76:77], v[4:5], v[40:41] op_sel:[0,1,1] op_sel_hi:[1,1,0]
	v_mfma_f32_16x16x32_f16 v[34:37], v[176:179], v[202:205], v[34:37]
	v_cvt_pk_f16_f32 v39, v66, v5
	v_pk_mul_f32 v[4:5], v[42:43], v[212:213] op_sel_hi:[1,0]
	s_nop 0
	v_pk_fma_f32 v[40:41], v[42:43], v[6:7], v[4:5] op_sel:[0,0,1] op_sel_hi:[1,1,0] neg_lo:[0,0,1] neg_hi:[0,0,1]
	v_pk_fma_f32 v[4:5], v[42:43], v[6:7], v[4:5] op_sel:[0,0,1] op_sel_hi:[1,0,0]
	v_mfma_f32_16x16x32_f16 v[62:65], v[148:151], v[206:209], v[110:113]
	v_cvt_pk_f16_f32 v40, v40, v5
	v_pk_mul_f32 v[4:5], v[44:45], v[56:57] op_sel_hi:[1,0]
	s_nop 0
	v_pk_fma_f32 v[6:7], v[44:45], v[86:87], v[4:5] op_sel:[0,0,1] op_sel_hi:[1,0,0] neg_lo:[0,0,1] neg_hi:[0,0,1]
	v_pk_fma_f32 v[4:5], v[44:45], v[86:87], v[4:5] op_sel:[0,0,1] op_sel_hi:[1,0,0]
	v_mfma_f32_16x16x32_f16 v[78:81], v[172:175], v[206:209], v[94:97]
	v_cvt_pk_f16_f32 v41, v6, v5
	v_lshl_add_u64 v[4:5], s[12:13], 0, v[54:55]
	v_lshl_add_u64 v[4:5], v[4:5], 0, v[16:17]
	v_lshl_add_u64 v[4:5], v[4:5], 0, v[138:139]
	global_store_dwordx4 v[4:5], v[38:41], off sc1
	s_waitcnt vmcnt(7)
	v_pk_mul_f32 v[4:5], v[22:23], v[8:9] op_sel_hi:[1,0]
	v_mfma_f32_16x16x32_f16 v[50:53], v[176:179], v[206:209], v[98:101]
	s_waitcnt vmcnt(6)
	v_pk_fma_f32 v[6:7], v[22:23], v[0:1], v[4:5] op_sel:[0,0,1] op_sel_hi:[1,1,0] neg_lo:[0,0,1] neg_hi:[0,0,1]
	v_pk_fma_f32 v[4:5], v[22:23], v[0:1], v[4:5] op_sel:[0,0,1] op_sel_hi:[1,0,0]
	v_mov_b32_e32 v38, v3
	v_cvt_pk_f16_f32 v4, v6, v5
	v_pk_mul_f32 v[6:7], v[24:25], v[8:9] op_sel:[0,1]
	s_nop 0
	v_pk_fma_f32 v[22:23], v[24:25], v[0:1], v[6:7] op_sel:[0,1,1] op_sel_hi:[1,1,0] neg_lo:[0,0,1] neg_hi:[0,0,1]
	v_pk_fma_f32 v[6:7], v[24:25], v[0:1], v[6:7] op_sel:[0,1,1] op_sel_hi:[1,1,0]
	s_nop 0
	v_cvt_pk_f16_f32 v5, v22, v7
	v_pk_mul_f32 v[6:7], v[82:83], v[10:11] op_sel_hi:[1,0]
	s_nop 0
	v_pk_fma_f32 v[22:23], v[82:83], v[2:3], v[6:7] op_sel:[0,0,1] op_sel_hi:[1,1,0] neg_lo:[0,0,1] neg_hi:[0,0,1]
	v_pk_fma_f32 v[6:7], v[82:83], v[2:3], v[6:7] op_sel:[0,0,1] op_sel_hi:[1,0,0]
	s_nop 0
	v_cvt_pk_f16_f32 v6, v22, v7
	v_mov_b32_e32 v22, v11
	v_pk_mul_f32 v[24:25], v[84:85], v[22:23] op_sel_hi:[1,0]
	s_nop 0
	v_pk_fma_f32 v[40:41], v[84:85], v[38:39], v[24:25] op_sel:[0,0,1] op_sel_hi:[1,0,0] neg_lo:[0,0,1] neg_hi:[0,0,1]
	v_pk_fma_f32 v[24:25], v[84:85], v[38:39], v[24:25] op_sel:[0,0,1] op_sel_hi:[1,0,0]
	s_nop 0
	v_cvt_pk_f16_f32 v7, v40, v25
	v_lshlrev_b64 v[24:25], 1, v[118:119]
	v_lshl_add_u64 v[40:41], s[10:11], 0, v[24:25]
	v_lshl_add_u64 v[40:41], v[40:41], 0, v[16:17]
	v_lshl_add_u64 v[40:41], v[40:41], 0, v[138:139]
	global_store_dwordx4 v[40:41], v[4:7], off sc1
	s_nop 1
	v_pk_mul_f32 v[4:5], v[30:31], v[8:9] op_sel_hi:[1,0]
	s_nop 0
	v_pk_fma_f32 v[6:7], v[30:31], v[0:1], v[4:5] op_sel:[0,0,1] op_sel_hi:[1,1,0] neg_lo:[0,0,1] neg_hi:[0,0,1]
	v_pk_fma_f32 v[4:5], v[30:31], v[0:1], v[4:5] op_sel:[0,0,1] op_sel_hi:[1,0,0]
	s_nop 0
	v_cvt_pk_f16_f32 v4, v6, v5
	v_pk_mul_f32 v[6:7], v[32:33], v[8:9] op_sel:[0,1]
	s_nop 0
	v_pk_fma_f32 v[8:9], v[32:33], v[0:1], v[6:7] op_sel:[0,1,1] op_sel_hi:[1,1,0] neg_lo:[0,0,1] neg_hi:[0,0,1]
	v_pk_fma_f32 v[0:1], v[32:33], v[0:1], v[6:7] op_sel:[0,1,1] op_sel_hi:[1,1,0]
	s_nop 0
	v_cvt_pk_f16_f32 v5, v8, v1
	v_pk_mul_f32 v[0:1], v[26:27], v[10:11] op_sel_hi:[1,0]
	s_nop 0
	v_pk_fma_f32 v[6:7], v[26:27], v[2:3], v[0:1] op_sel:[0,0,1] op_sel_hi:[1,1,0] neg_lo:[0,0,1] neg_hi:[0,0,1]
	v_pk_fma_f32 v[0:1], v[26:27], v[2:3], v[0:1] op_sel:[0,0,1] op_sel_hi:[1,0,0]
	s_nop 0
	v_cvt_pk_f16_f32 v6, v6, v1
	v_pk_mul_f32 v[0:1], v[28:29], v[22:23] op_sel_hi:[1,0]
	s_nop 0
	v_pk_fma_f32 v[2:3], v[28:29], v[38:39], v[0:1] op_sel:[0,0,1] op_sel_hi:[1,0,0] neg_lo:[0,0,1] neg_hi:[0,0,1]
	v_pk_fma_f32 v[0:1], v[28:29], v[38:39], v[0:1] op_sel:[0,0,1] op_sel_hi:[1,0,0]
	v_cvt_pk_f16_f32 v3, v48, v49
	v_cvt_pk_f16_f32 v7, v2, v1
	v_lshl_add_u64 v[0:1], s[12:13], 0, v[24:25]
	v_lshl_add_u64 v[0:1], v[0:1], 0, v[16:17]
	v_lshl_add_u64 v[0:1], v[0:1], 0, v[138:139]
	global_store_dwordx4 v[0:1], v[4:7], off sc1
	v_lshlrev_b64 v[0:1], 18, v[18:19]
	v_lshlrev_b32_e32 v2, 7, v145
	v_lshl_add_u64 v[0:1], s[14:15], 0, v[0:1]
	v_and_b32_e32 v16, 0x3e000, v2
	v_lshl_add_u64 v[0:1], v[0:1], 0, v[16:17]
	v_lshlrev_b32_e32 v16, 4, v20
	v_lshl_add_u64 v[4:5], v[0:1], 0, v[16:17]
	v_lshlrev_b32_e32 v16, 12, v144
	v_cvt_pk_f16_f32 v2, v46, v47
	v_cvt_pk_f16_f32 v1, v72, v73
	v_cvt_pk_f16_f32 v0, v70, v71
	v_lshl_add_u64 v[4:5], v[4:5], 0, v[16:17]
	global_store_dwordx4 v[4:5], v[0:3], off sc1
	s_nop 1
	v_cvt_pk_f16_f32 v3, v36, v37
	v_cvt_pk_f16_f32 v2, v34, v35
	v_cvt_pk_f16_f32 v1, v60, v61
	v_cvt_pk_f16_f32 v0, v58, v59
	global_store_dwordx4 v[4:5], v[0:3], off offset:1024 sc1
	s_nop 1
	v_cvt_pk_f16_f32 v3, v64, v65
	v_cvt_pk_f16_f32 v2, v62, v63
	v_cvt_pk_f16_f32 v1, v14, v15
	v_cvt_pk_f16_f32 v0, v12, v13
	global_store_dwordx4 v[4:5], v[0:3], off offset:2048 sc1
	s_nop 1
	v_cvt_pk_f16_f32 v3, v52, v53
	v_cvt_pk_f16_f32 v2, v50, v51
	v_cvt_pk_f16_f32 v1, v80, v81
	v_cvt_pk_f16_f32 v0, v78, v79
	global_store_dwordx4 v[4:5], v[0:3], off offset:3072 sc1
	s_endpgm
	.p2align	8
